# grid barriers at the out-proj->q-proj and attention->o-proj seams replaced by a 4-workgroup panel rendezvous (same 64x4 tile map on both sides)
# baseline (speedup 1.0000x reference)
; __device__ __forceinline__ unsigned xb_ld(unsigned* p)              { return __hip_atomic_load(p, __ATOMIC_RELAXED, __HIP_MEMORY_SCOPE_AGENT); }
; __device__ __forceinline__ unsigned xb_add(unsigned* p, unsigned v) { return __hip_atomic_fetch_add(p, v, __ATOMIC_RELAXED, __HIP_MEMORY_SCOPE_AGENT); }
; #define XB_SPIN(cond, bar) do { unsigned _sp = 0; while (cond) { __builtin_amdgcn_s_sleep(1); \
;     if ((++_sp & 255u) == 0u) { if (xb_ld(&(bar)[XB_TMO])) break; if (_sp > XB_SPIN_CAP) { atomicAdd(&(bar)[XB_TMO], 1u); break; } } } } while (0)
; __device__ __forceinline__ void xcd_barrier(const XcdBarrier& b) {
;     asm volatile("s_waitcnt vmcnt(0)" ::: "memory");
;     __syncthreads();
;     if (threadIdx.x == 0) {
;         unsigned* bar = b.bar;
;         __builtin_amdgcn_s_waitcnt(0);
;         unsigned nloc = b.st[0], nx = b.st[1];
;         if (nloc == 0u) { xcd_barrier_complete(bar, b.x, nloc, nx); b.st[0] = nloc; b.st[1] = nx; }
;         const unsigned old = xb_add(&bar[XB_XSUB(b.x)], 1u);
;         const unsigned gen = old / nloc;
;         if (old + 1u == (gen + 1u) * nloc) {
;             __builtin_amdgcn_fence(__ATOMIC_RELEASE, "agent");
;             asm volatile("s_waitcnt vmcnt(0)" ::: "memory");
;             const unsigned og = xb_add(&bar[XB_TOP], 1u);
;             const unsigned tg = og / nx;
;             if (og + 1u == (tg + 1u) * nx) xb_add(&bar[XB_TOPGEN], 1u);
;             else XB_SPIN(xb_ld(&bar[XB_TOPGEN]) == tg, bar);
;             __builtin_amdgcn_fence(__ATOMIC_ACQUIRE, "agent");
;             xb_add(&bar[XB_XGEN(b.x)], 1u);
;             asm volatile("s_waitcnt vmcnt(0)" ::: "memory");
;         } else {
;             XB_SPIN(xb_ld(&bar[XB_XGEN(b.x)]) == gen, bar);
;             __builtin_amdgcn_fence(__ATOMIC_ACQUIRE, "agent");
;             asm volatile("s_waitcnt vmcnt(0)" ::: "memory");
;         }
;     }
;     __syncthreads();
; }
.LBB0_2371:
	s_cmp_gt_i32 s75, 6
	s_cselect_b64 s[4:5], -1, 0
	s_and_b64 s[0:1], s[0:1], s[4:5]
	s_andn2_b64 vcc, exec, s[0:1]
	s_cbranch_vccnz .LBB0_2425
	s_waitcnt vmcnt(0)
	s_waitcnt vmcnt(0) lgkmcnt(0)
	s_barrier
	s_and_saveexec_b64 s[0:1], s[72:73]
	s_cbranch_execz .LBB0_2424
	buffer_wbl2 sc1
	s_waitcnt vmcnt(0)
	s_and_b32 s3, s2, 63
	s_lshl_b32 s3, s3, 6
	s_add_u32 s6, s24, s3
	s_addc_u32 s7, s25, 0
	s_add_u32 s6, s6, 0x40000
	s_addc_u32 s7, s7, 0
	v_mov_b32_e32 v1, 0
	v_mov_b32_e32 v2, 1
	global_atomic_add v1, v2, s[6:7]
	s_mov_b32 s8, 0
.Lpan_spin0:
	global_load_dword v3, v1, s[6:7] sc1
	s_waitcnt vmcnt(0)
	v_cmp_gt_u32_e32 vcc, 4, v3
	s_cbranch_vccz .Lpan_done0
	s_sleep 1
	s_add_i32 s8, s8, 1
	s_cmp_lt_u32 s8, 0x200000
	s_cbranch_scc1 .Lpan_spin0
.Lpan_done0:
	buffer_inv sc1
	s_waitcnt vmcnt(0)
	s_branch .LBB0_2424
	s_add_i32 s3, 0, 0x27c20
	v_mov_b32_e32 v1, s3
	s_waitcnt vmcnt(0) expcnt(0) lgkmcnt(0)
	ds_read_b32 v3, v1
	s_add_i32 s3, 0, 0x27c24
	v_mov_b32_e32 v1, s3
	ds_read_b32 v1, v1
	s_waitcnt lgkmcnt(1)
	v_cmp_ne_u32_e32 vcc, 0, v3
	s_cbranch_vccnz .LBB0_2388
	v_readlane_b32 s6, v254, 0
	v_readlane_b32 s7, v254, 1
	s_load_dwordx2 s[10:11], s[6:7], 0x4
	s_add_u32 s6, s24, 0x4200
	s_addc_u32 s7, s25, 0
	s_add_u32 s8, s24, 0x4400
	s_addc_u32 s9, s25, 0
	s_waitcnt lgkmcnt(0)
	s_mul_i32 s3, s10, s26
	s_add_u32 s10, s24, 0x4500
	s_mul_i32 s3, s3, s11
	s_addc_u32 s11, s25, 0
	s_add_u32 s12, s24, 0x4600
	s_addc_u32 s13, s25, 0
	s_add_u32 s14, s24, 0x4700
	s_addc_u32 s15, s25, 0
	s_add_u32 s16, s24, 0x4800
	s_addc_u32 s17, s25, 0
	s_add_u32 s18, s24, 0x4900
	s_addc_u32 s19, s25, 0
	s_add_u32 s20, s24, 0x4a00
	s_addc_u32 s21, s25, 0
	s_add_u32 s22, s24, 0x4b00
	s_addc_u32 s23, s25, 0
	s_add_u32 s28, s24, 0x4c00
	s_addc_u32 s29, s25, 0
	s_add_u32 s30, s24, 0x4d00
	s_addc_u32 s31, s25, 0
	s_add_u32 s34, s24, 0x4e00
	s_addc_u32 s35, s25, 0
	s_add_u32 s36, s24, 0x4f00
	s_addc_u32 s37, s25, 0
	s_add_u32 s38, s24, 0x5000
	s_addc_u32 s39, s25, 0
	s_add_u32 s40, s24, 0x5100
	s_addc_u32 s41, s25, 0
	s_add_u32 s42, s24, 0x5200
	s_addc_u32 s43, s25, 0
	s_add_u32 s44, s24, 0x5300
	s_addc_u32 s45, s25, 0
	s_mov_b32 s27, 1
	v_mov_b32_e32 v17, 0
	s_branch .LBB0_2376

; __device__ __forceinline__ unsigned xb_ld(unsigned* p)              { return __hip_atomic_load(p, __ATOMIC_RELAXED, __HIP_MEMORY_SCOPE_AGENT); }
; __device__ __forceinline__ unsigned xb_add(unsigned* p, unsigned v) { return __hip_atomic_fetch_add(p, v, __ATOMIC_RELAXED, __HIP_MEMORY_SCOPE_AGENT); }
; #define XB_SPIN(cond, bar) do { unsigned _sp = 0; while (cond) { __builtin_amdgcn_s_sleep(1); \
;     if ((++_sp & 255u) == 0u) { if (xb_ld(&(bar)[XB_TMO])) break; if (_sp > XB_SPIN_CAP) { atomicAdd(&(bar)[XB_TMO], 1u); break; } } } } while (0)
; __device__ __forceinline__ void xcd_barrier(const XcdBarrier& b) {
;     asm volatile("s_waitcnt vmcnt(0)" ::: "memory");
;     __syncthreads();
;     if (threadIdx.x == 0) {
;         unsigned* bar = b.bar;
;         __builtin_amdgcn_s_waitcnt(0);
;         unsigned nloc = b.st[0], nx = b.st[1];
;         if (nloc == 0u) { xcd_barrier_complete(bar, b.x, nloc, nx); b.st[0] = nloc; b.st[1] = nx; }
;         const unsigned old = xb_add(&bar[XB_XSUB(b.x)], 1u);
;         const unsigned gen = old / nloc;
;         if (old + 1u == (gen + 1u) * nloc) {
;             __builtin_amdgcn_fence(__ATOMIC_RELEASE, "agent");
;             asm volatile("s_waitcnt vmcnt(0)" ::: "memory");
;             const unsigned og = xb_add(&bar[XB_TOP], 1u);
;             const unsigned tg = og / nx;
;             if (og + 1u == (tg + 1u) * nx) xb_add(&bar[XB_TOPGEN], 1u);
;             else XB_SPIN(xb_ld(&bar[XB_TOPGEN]) == tg, bar);
;             __builtin_amdgcn_fence(__ATOMIC_ACQUIRE, "agent");
;             xb_add(&bar[XB_XGEN(b.x)], 1u);
;             asm volatile("s_waitcnt vmcnt(0)" ::: "memory");
;         } else {
;             XB_SPIN(xb_ld(&bar[XB_XGEN(b.x)]) == gen, bar);
;             __builtin_amdgcn_fence(__ATOMIC_ACQUIRE, "agent");
;             asm volatile("s_waitcnt vmcnt(0)" ::: "memory");
;         }
;     }
;     __syncthreads();
; }
.LBB0_2448:
	s_cmp_lt_i32 s74, 8
	s_cselect_b64 s[4:5], -1, 0
	s_cmp_gt_i32 s75, 8
	s_cselect_b64 s[0:1], -1, 0
	s_and_b64 s[4:5], s[4:5], s[0:1]
	s_andn2_b64 vcc, exec, s[4:5]
	s_cbranch_vccnz .LBB0_2502
	s_waitcnt vmcnt(0)
	s_waitcnt vmcnt(0) lgkmcnt(0)
	s_barrier
	s_and_saveexec_b64 s[4:5], s[72:73]
	s_cbranch_execz .LBB0_2501
	buffer_wbl2 sc1
	s_waitcnt vmcnt(0)
	s_and_b32 s3, s2, 63
	s_lshl_b32 s3, s3, 6
	s_add_u32 s6, s24, s3
	s_addc_u32 s7, s25, 0
	s_add_u32 s6, s6, 0x44000
	s_addc_u32 s7, s7, 0
	v_mov_b32_e32 v1, 0
	v_mov_b32_e32 v2, 1
	global_atomic_add v1, v2, s[6:7]
	s_mov_b32 s8, 0
